# v031-bscatter-batched-hist-reduction
# speedup vs baseline: 1.1257x; 1.0239x over previous
.LBB1_20:
	s_or_b64 exec, exec, s[4:5]
	v_and_b32_e32 v10, 0x7f, v0
	s_movk_i32 s3, 0x62
	v_cmp_gt_u32_e32 vcc, s3, v10
	s_and_saveexec_b64 s[6:7], vcc
	s_cbranch_execz .LBB1_22
	s_load_dwordx2 s[4:5], s[0:1], 0x18
	v_lshrrev_b32_e32 v25, 7, v0
	v_lshlrev_b32_e32 v28, 4, v10
	s_movk_i32 s3, 0x620
	v_readfirstlane_b32 s12, v0
	v_mad_u32_u24 v25, v25, s3, v28
	s_lshr_b32 s12, s12, 7
	s_lshl_b32 s13, s12, 6
	s_mul_i32 s14, s13, 0x620
	s_sub_i32 s15, s2, s13
	v_mov_b32_e32 v30, 0
	v_mov_b32_e32 v31, 0
	v_mov_b32_e32 v32, 0
	v_mov_b32_e32 v33, 0
	v_mov_b32_e32 v10, 0
	v_mov_b32_e32 v11, 0
	v_mov_b32_e32 v12, 0
	v_mov_b32_e32 v13, 0
	s_waitcnt lgkmcnt(0)
	s_add_u32 s4, s4, s14
	s_addc_u32 s5, s5, 0
	global_load_dwordx4 v[68:71], v28, s[4:5]
	global_load_dwordx4 v[72:75], v28, s[4:5] offset:1568
	s_add_u32 s4, s4, 0xc40
	s_addc_u32 s5, s5, 0
	global_load_dwordx4 v[76:79], v28, s[4:5]
	global_load_dwordx4 v[80:83], v28, s[4:5] offset:1568
	s_add_u32 s4, s4, 0xc40
	s_addc_u32 s5, s5, 0
	global_load_dwordx4 v[84:87], v28, s[4:5]
	global_load_dwordx4 v[88:91], v28, s[4:5] offset:1568
	s_add_u32 s4, s4, 0xc40
	s_addc_u32 s5, s5, 0
	global_load_dwordx4 v[92:95], v28, s[4:5]
	global_load_dwordx4 v[96:99], v28, s[4:5] offset:1568
	s_add_u32 s4, s4, 0xc40
	s_addc_u32 s5, s5, 0
	global_load_dwordx4 v[100:103], v28, s[4:5]
	global_load_dwordx4 v[104:107], v28, s[4:5] offset:1568
	s_add_u32 s4, s4, 0xc40
	s_addc_u32 s5, s5, 0
	global_load_dwordx4 v[108:111], v28, s[4:5]
	global_load_dwordx4 v[112:115], v28, s[4:5] offset:1568
	s_add_u32 s4, s4, 0xc40
	s_addc_u32 s5, s5, 0
	global_load_dwordx4 v[116:119], v28, s[4:5]
	global_load_dwordx4 v[120:123], v28, s[4:5] offset:1568
	s_add_u32 s4, s4, 0xc40
	s_addc_u32 s5, s5, 0
	global_load_dwordx4 v[124:127], v28, s[4:5]
	global_load_dwordx4 v[128:131], v28, s[4:5] offset:1568
	s_add_u32 s4, s4, 0xc40
	s_addc_u32 s5, s5, 0
	global_load_dwordx4 v[132:135], v28, s[4:5]
	global_load_dwordx4 v[136:139], v28, s[4:5] offset:1568
	s_add_u32 s4, s4, 0xc40
	s_addc_u32 s5, s5, 0
	global_load_dwordx4 v[140:143], v28, s[4:5]
	global_load_dwordx4 v[144:147], v28, s[4:5] offset:1568
	s_add_u32 s4, s4, 0xc40
	s_addc_u32 s5, s5, 0
	global_load_dwordx4 v[148:151], v28, s[4:5]
	global_load_dwordx4 v[152:155], v28, s[4:5] offset:1568
	s_add_u32 s4, s4, 0xc40
	s_addc_u32 s5, s5, 0
	global_load_dwordx4 v[156:159], v28, s[4:5]
	global_load_dwordx4 v[160:163], v28, s[4:5] offset:1568
	s_add_u32 s4, s4, 0xc40
	s_addc_u32 s5, s5, 0
	global_load_dwordx4 v[164:167], v28, s[4:5]
	global_load_dwordx4 v[168:171], v28, s[4:5] offset:1568
	s_add_u32 s4, s4, 0xc40
	s_addc_u32 s5, s5, 0
	global_load_dwordx4 v[172:175], v28, s[4:5]
	global_load_dwordx4 v[176:179], v28, s[4:5] offset:1568
	s_add_u32 s4, s4, 0xc40
	s_addc_u32 s5, s5, 0
	global_load_dwordx4 v[180:183], v28, s[4:5]
	global_load_dwordx4 v[184:187], v28, s[4:5] offset:1568
	s_add_u32 s4, s4, 0xc40
	s_addc_u32 s5, s5, 0
	global_load_dwordx4 v[188:191], v28, s[4:5]
	global_load_dwordx4 v[192:195], v28, s[4:5] offset:1568
	s_add_u32 s4, s4, 0xc40
	s_addc_u32 s5, s5, 0
	s_waitcnt vmcnt(0)
	v_add3_u32 v30, v30, v68, v72
	v_add3_u32 v31, v31, v69, v73
	v_add3_u32 v32, v32, v70, v74
	v_add3_u32 v33, v33, v71, v75
	v_add3_u32 v30, v30, v76, v80
	v_add3_u32 v31, v31, v77, v81
	v_add3_u32 v32, v32, v78, v82
	v_add3_u32 v33, v33, v79, v83
	v_add3_u32 v30, v30, v84, v88
	v_add3_u32 v31, v31, v85, v89
	v_add3_u32 v32, v32, v86, v90
	v_add3_u32 v33, v33, v87, v91
	v_add3_u32 v30, v30, v92, v96
	v_add3_u32 v31, v31, v93, v97
	v_add3_u32 v32, v32, v94, v98
	v_add3_u32 v33, v33, v95, v99
	v_add3_u32 v30, v30, v100, v104
	v_add3_u32 v31, v31, v101, v105
	v_add3_u32 v32, v32, v102, v106
	v_add3_u32 v33, v33, v103, v107
	v_add3_u32 v30, v30, v108, v112
	v_add3_u32 v31, v31, v109, v113
	v_add3_u32 v32, v32, v110, v114
	v_add3_u32 v33, v33, v111, v115
	v_add3_u32 v30, v30, v116, v120
	v_add3_u32 v31, v31, v117, v121
	v_add3_u32 v32, v32, v118, v122
	v_add3_u32 v33, v33, v119, v123
	v_add3_u32 v30, v30, v124, v128
	v_add3_u32 v31, v31, v125, v129
	v_add3_u32 v32, v32, v126, v130
	v_add3_u32 v33, v33, v127, v131
	v_add3_u32 v30, v30, v132, v136
	v_add3_u32 v31, v31, v133, v137
	v_add3_u32 v32, v32, v134, v138
	v_add3_u32 v33, v33, v135, v139
	v_add3_u32 v30, v30, v140, v144
	v_add3_u32 v31, v31, v141, v145
	v_add3_u32 v32, v32, v142, v146
	v_add3_u32 v33, v33, v143, v147
	v_add3_u32 v30, v30, v148, v152
	v_add3_u32 v31, v31, v149, v153
	v_add3_u32 v32, v32, v150, v154
	v_add3_u32 v33, v33, v151, v155
	v_add3_u32 v30, v30, v156, v160
	v_add3_u32 v31, v31, v157, v161
	v_add3_u32 v32, v32, v158, v162
	v_add3_u32 v33, v33, v159, v163
	v_add3_u32 v30, v30, v164, v168
	v_add3_u32 v31, v31, v165, v169
	v_add3_u32 v32, v32, v166, v170
	v_add3_u32 v33, v33, v167, v171
	v_add3_u32 v30, v30, v172, v176
	v_add3_u32 v31, v31, v173, v177
	v_add3_u32 v32, v32, v174, v178
	v_add3_u32 v33, v33, v175, v179
	v_add3_u32 v30, v30, v180, v184
	v_add3_u32 v31, v31, v181, v185
	v_add3_u32 v32, v32, v182, v186
	v_add3_u32 v33, v33, v183, v187
	v_add3_u32 v30, v30, v188, v192
	v_add3_u32 v31, v31, v189, v193
	v_add3_u32 v32, v32, v190, v194
	v_add3_u32 v33, v33, v191, v195
	s_cmp_gt_i32 s15, 0
	s_cbranch_scc0 .Lbscat_nopre_0
	s_cmp_lt_i32 s15, 64
	s_cbranch_scc0 .Lbscat_nopre_0
	s_cmp_gt_i32 s15, 0
	s_cselect_b32 s16, 1, 0
	v_mad_u32_u24 v10, v68, s16, v10
	v_mad_u32_u24 v11, v69, s16, v11
	v_mad_u32_u24 v12, v70, s16, v12
	v_mad_u32_u24 v13, v71, s16, v13
	s_cmp_gt_i32 s15, 1
	s_cselect_b32 s16, 1, 0
	v_mad_u32_u24 v10, v72, s16, v10
	v_mad_u32_u24 v11, v73, s16, v11
	v_mad_u32_u24 v12, v74, s16, v12
	v_mad_u32_u24 v13, v75, s16, v13
	s_cmp_gt_i32 s15, 2
	s_cselect_b32 s16, 1, 0
	v_mad_u32_u24 v10, v76, s16, v10
	v_mad_u32_u24 v11, v77, s16, v11
	v_mad_u32_u24 v12, v78, s16, v12
	v_mad_u32_u24 v13, v79, s16, v13
	s_cmp_gt_i32 s15, 3
	s_cselect_b32 s16, 1, 0
	v_mad_u32_u24 v10, v80, s16, v10
	v_mad_u32_u24 v11, v81, s16, v11
	v_mad_u32_u24 v12, v82, s16, v12
	v_mad_u32_u24 v13, v83, s16, v13
	s_cmp_gt_i32 s15, 4
	s_cselect_b32 s16, 1, 0
	v_mad_u32_u24 v10, v84, s16, v10
	v_mad_u32_u24 v11, v85, s16, v11
	v_mad_u32_u24 v12, v86, s16, v12
	v_mad_u32_u24 v13, v87, s16, v13
	s_cmp_gt_i32 s15, 5
	s_cselect_b32 s16, 1, 0
	v_mad_u32_u24 v10, v88, s16, v10
	v_mad_u32_u24 v11, v89, s16, v11
	v_mad_u32_u24 v12, v90, s16, v12
	v_mad_u32_u24 v13, v91, s16, v13
	s_cmp_gt_i32 s15, 6
	s_cselect_b32 s16, 1, 0
	v_mad_u32_u24 v10, v92, s16, v10
	v_mad_u32_u24 v11, v93, s16, v11
	v_mad_u32_u24 v12, v94, s16, v12
	v_mad_u32_u24 v13, v95, s16, v13
	s_cmp_gt_i32 s15, 7
	s_cselect_b32 s16, 1, 0
	v_mad_u32_u24 v10, v96, s16, v10
	v_mad_u32_u24 v11, v97, s16, v11
	v_mad_u32_u24 v12, v98, s16, v12
	v_mad_u32_u24 v13, v99, s16, v13
	s_cmp_gt_i32 s15, 8
	s_cselect_b32 s16, 1, 0
	v_mad_u32_u24 v10, v100, s16, v10
	v_mad_u32_u24 v11, v101, s16, v11
	v_mad_u32_u24 v12, v102, s16, v12
	v_mad_u32_u24 v13, v103, s16, v13
	s_cmp_gt_i32 s15, 9
	s_cselect_b32 s16, 1, 0
	v_mad_u32_u24 v10, v104, s16, v10
	v_mad_u32_u24 v11, v105, s16, v11
	v_mad_u32_u24 v12, v106, s16, v12
	v_mad_u32_u24 v13, v107, s16, v13
	s_cmp_gt_i32 s15, 10
	s_cselect_b32 s16, 1, 0
	v_mad_u32_u24 v10, v108, s16, v10
	v_mad_u32_u24 v11, v109, s16, v11
	v_mad_u32_u24 v12, v110, s16, v12
	v_mad_u32_u24 v13, v111, s16, v13
	s_cmp_gt_i32 s15, 11
	s_cselect_b32 s16, 1, 0
	v_mad_u32_u24 v10, v112, s16, v10
	v_mad_u32_u24 v11, v113, s16, v11
	v_mad_u32_u24 v12, v114, s16, v12
	v_mad_u32_u24 v13, v115, s16, v13
	s_cmp_gt_i32 s15, 12
	s_cselect_b32 s16, 1, 0
	v_mad_u32_u24 v10, v116, s16, v10
	v_mad_u32_u24 v11, v117, s16, v11
	v_mad_u32_u24 v12, v118, s16, v12
	v_mad_u32_u24 v13, v119, s16, v13
	s_cmp_gt_i32 s15, 13
	s_cselect_b32 s16, 1, 0
	v_mad_u32_u24 v10, v120, s16, v10
	v_mad_u32_u24 v11, v121, s16, v11
	v_mad_u32_u24 v12, v122, s16, v12
	v_mad_u32_u24 v13, v123, s16, v13
	s_cmp_gt_i32 s15, 14
	s_cselect_b32 s16, 1, 0
	v_mad_u32_u24 v10, v124, s16, v10
	v_mad_u32_u24 v11, v125, s16, v11
	v_mad_u32_u24 v12, v126, s16, v12
	v_mad_u32_u24 v13, v127, s16, v13
	s_cmp_gt_i32 s15, 15
	s_cselect_b32 s16, 1, 0
	v_mad_u32_u24 v10, v128, s16, v10
	v_mad_u32_u24 v11, v129, s16, v11
	v_mad_u32_u24 v12, v130, s16, v12
	v_mad_u32_u24 v13, v131, s16, v13
	s_cmp_gt_i32 s15, 16
	s_cselect_b32 s16, 1, 0
	v_mad_u32_u24 v10, v132, s16, v10
	v_mad_u32_u24 v11, v133, s16, v11
	v_mad_u32_u24 v12, v134, s16, v12
	v_mad_u32_u24 v13, v135, s16, v13
	s_cmp_gt_i32 s15, 17
	s_cselect_b32 s16, 1, 0
	v_mad_u32_u24 v10, v136, s16, v10
	v_mad_u32_u24 v11, v137, s16, v11
	v_mad_u32_u24 v12, v138, s16, v12
	v_mad_u32_u24 v13, v139, s16, v13
	s_cmp_gt_i32 s15, 18
	s_cselect_b32 s16, 1, 0
	v_mad_u32_u24 v10, v140, s16, v10
	v_mad_u32_u24 v11, v141, s16, v11
	v_mad_u32_u24 v12, v142, s16, v12
	v_mad_u32_u24 v13, v143, s16, v13
	s_cmp_gt_i32 s15, 19
	s_cselect_b32 s16, 1, 0
	v_mad_u32_u24 v10, v144, s16, v10
	v_mad_u32_u24 v11, v145, s16, v11
	v_mad_u32_u24 v12, v146, s16, v12
	v_mad_u32_u24 v13, v147, s16, v13
	s_cmp_gt_i32 s15, 20
	s_cselect_b32 s16, 1, 0
	v_mad_u32_u24 v10, v148, s16, v10
	v_mad_u32_u24 v11, v149, s16, v11
	v_mad_u32_u24 v12, v150, s16, v12
	v_mad_u32_u24 v13, v151, s16, v13
	s_cmp_gt_i32 s15, 21
	s_cselect_b32 s16, 1, 0
	v_mad_u32_u24 v10, v152, s16, v10
	v_mad_u32_u24 v11, v153, s16, v11
	v_mad_u32_u24 v12, v154, s16, v12
	v_mad_u32_u24 v13, v155, s16, v13
	s_cmp_gt_i32 s15, 22
	s_cselect_b32 s16, 1, 0
	v_mad_u32_u24 v10, v156, s16, v10
	v_mad_u32_u24 v11, v157, s16, v11
	v_mad_u32_u24 v12, v158, s16, v12
	v_mad_u32_u24 v13, v159, s16, v13
	s_cmp_gt_i32 s15, 23
	s_cselect_b32 s16, 1, 0
	v_mad_u32_u24 v10, v160, s16, v10
	v_mad_u32_u24 v11, v161, s16, v11
	v_mad_u32_u24 v12, v162, s16, v12
	v_mad_u32_u24 v13, v163, s16, v13
	s_cmp_gt_i32 s15, 24
	s_cselect_b32 s16, 1, 0
	v_mad_u32_u24 v10, v164, s16, v10
	v_mad_u32_u24 v11, v165, s16, v11
	v_mad_u32_u24 v12, v166, s16, v12
	v_mad_u32_u24 v13, v167, s16, v13
	s_cmp_gt_i32 s15, 25
	s_cselect_b32 s16, 1, 0
	v_mad_u32_u24 v10, v168, s16, v10
	v_mad_u32_u24 v11, v169, s16, v11
	v_mad_u32_u24 v12, v170, s16, v12
	v_mad_u32_u24 v13, v171, s16, v13
	s_cmp_gt_i32 s15, 26
	s_cselect_b32 s16, 1, 0
	v_mad_u32_u24 v10, v172, s16, v10
	v_mad_u32_u24 v11, v173, s16, v11
	v_mad_u32_u24 v12, v174, s16, v12
	v_mad_u32_u24 v13, v175, s16, v13
	s_cmp_gt_i32 s15, 27
	s_cselect_b32 s16, 1, 0
	v_mad_u32_u24 v10, v176, s16, v10
	v_mad_u32_u24 v11, v177, s16, v11
	v_mad_u32_u24 v12, v178, s16, v12
	v_mad_u32_u24 v13, v179, s16, v13
	s_cmp_gt_i32 s15, 28
	s_cselect_b32 s16, 1, 0
	v_mad_u32_u24 v10, v180, s16, v10
	v_mad_u32_u24 v11, v181, s16, v11
	v_mad_u32_u24 v12, v182, s16, v12
	v_mad_u32_u24 v13, v183, s16, v13
	s_cmp_gt_i32 s15, 29
	s_cselect_b32 s16, 1, 0
	v_mad_u32_u24 v10, v184, s16, v10
	v_mad_u32_u24 v11, v185, s16, v11
	v_mad_u32_u24 v12, v186, s16, v12
	v_mad_u32_u24 v13, v187, s16, v13
	s_cmp_gt_i32 s15, 30
	s_cselect_b32 s16, 1, 0
	v_mad_u32_u24 v10, v188, s16, v10
	v_mad_u32_u24 v11, v189, s16, v11
	v_mad_u32_u24 v12, v190, s16, v12
	v_mad_u32_u24 v13, v191, s16, v13
	s_cmp_gt_i32 s15, 31
	s_cselect_b32 s16, 1, 0
	v_mad_u32_u24 v10, v192, s16, v10
	v_mad_u32_u24 v11, v193, s16, v11
	v_mad_u32_u24 v12, v194, s16, v12
	v_mad_u32_u24 v13, v195, s16, v13
.Lbscat_nopre_0:
	global_load_dwordx4 v[68:71], v28, s[4:5]
	global_load_dwordx4 v[72:75], v28, s[4:5] offset:1568
	s_add_u32 s4, s4, 0xc40
	s_addc_u32 s5, s5, 0
	global_load_dwordx4 v[76:79], v28, s[4:5]
	global_load_dwordx4 v[80:83], v28, s[4:5] offset:1568
	s_add_u32 s4, s4, 0xc40
	s_addc_u32 s5, s5, 0
	global_load_dwordx4 v[84:87], v28, s[4:5]
	global_load_dwordx4 v[88:91], v28, s[4:5] offset:1568
	s_add_u32 s4, s4, 0xc40
	s_addc_u32 s5, s5, 0
	global_load_dwordx4 v[92:95], v28, s[4:5]
	global_load_dwordx4 v[96:99], v28, s[4:5] offset:1568
	s_add_u32 s4, s4, 0xc40
	s_addc_u32 s5, s5, 0
	global_load_dwordx4 v[100:103], v28, s[4:5]
	global_load_dwordx4 v[104:107], v28, s[4:5] offset:1568
	s_add_u32 s4, s4, 0xc40
	s_addc_u32 s5, s5, 0
	global_load_dwordx4 v[108:111], v28, s[4:5]
	global_load_dwordx4 v[112:115], v28, s[4:5] offset:1568
	s_add_u32 s4, s4, 0xc40
	s_addc_u32 s5, s5, 0
	global_load_dwordx4 v[116:119], v28, s[4:5]
	global_load_dwordx4 v[120:123], v28, s[4:5] offset:1568
	s_add_u32 s4, s4, 0xc40
	s_addc_u32 s5, s5, 0
	global_load_dwordx4 v[124:127], v28, s[4:5]
	global_load_dwordx4 v[128:131], v28, s[4:5] offset:1568
	s_add_u32 s4, s4, 0xc40
	s_addc_u32 s5, s5, 0
	global_load_dwordx4 v[132:135], v28, s[4:5]
	global_load_dwordx4 v[136:139], v28, s[4:5] offset:1568
	s_add_u32 s4, s4, 0xc40
	s_addc_u32 s5, s5, 0
	global_load_dwordx4 v[140:143], v28, s[4:5]
	global_load_dwordx4 v[144:147], v28, s[4:5] offset:1568
	s_add_u32 s4, s4, 0xc40
	s_addc_u32 s5, s5, 0
	global_load_dwordx4 v[148:151], v28, s[4:5]
	global_load_dwordx4 v[152:155], v28, s[4:5] offset:1568
	s_add_u32 s4, s4, 0xc40
	s_addc_u32 s5, s5, 0
	global_load_dwordx4 v[156:159], v28, s[4:5]
	global_load_dwordx4 v[160:163], v28, s[4:5] offset:1568
	s_add_u32 s4, s4, 0xc40
	s_addc_u32 s5, s5, 0
	global_load_dwordx4 v[164:167], v28, s[4:5]
	global_load_dwordx4 v[168:171], v28, s[4:5] offset:1568
	s_add_u32 s4, s4, 0xc40
	s_addc_u32 s5, s5, 0
	global_load_dwordx4 v[172:175], v28, s[4:5]
	global_load_dwordx4 v[176:179], v28, s[4:5] offset:1568
	s_add_u32 s4, s4, 0xc40
	s_addc_u32 s5, s5, 0
	global_load_dwordx4 v[180:183], v28, s[4:5]
	global_load_dwordx4 v[184:187], v28, s[4:5] offset:1568
	s_add_u32 s4, s4, 0xc40
	s_addc_u32 s5, s5, 0
	global_load_dwordx4 v[188:191], v28, s[4:5]
	global_load_dwordx4 v[192:195], v28, s[4:5] offset:1568
	s_add_u32 s4, s4, 0xc40
	s_addc_u32 s5, s5, 0
	s_waitcnt vmcnt(0)
	v_add3_u32 v30, v30, v68, v72
	v_add3_u32 v31, v31, v69, v73
	v_add3_u32 v32, v32, v70, v74
	v_add3_u32 v33, v33, v71, v75
	v_add3_u32 v30, v30, v76, v80
	v_add3_u32 v31, v31, v77, v81
	v_add3_u32 v32, v32, v78, v82
	v_add3_u32 v33, v33, v79, v83
	v_add3_u32 v30, v30, v84, v88
	v_add3_u32 v31, v31, v85, v89
	v_add3_u32 v32, v32, v86, v90
	v_add3_u32 v33, v33, v87, v91
	v_add3_u32 v30, v30, v92, v96
	v_add3_u32 v31, v31, v93, v97
	v_add3_u32 v32, v32, v94, v98
	v_add3_u32 v33, v33, v95, v99
	v_add3_u32 v30, v30, v100, v104
	v_add3_u32 v31, v31, v101, v105
	v_add3_u32 v32, v32, v102, v106
	v_add3_u32 v33, v33, v103, v107
	v_add3_u32 v30, v30, v108, v112
	v_add3_u32 v31, v31, v109, v113
	v_add3_u32 v32, v32, v110, v114
	v_add3_u32 v33, v33, v111, v115
	v_add3_u32 v30, v30, v116, v120
	v_add3_u32 v31, v31, v117, v121
	v_add3_u32 v32, v32, v118, v122
	v_add3_u32 v33, v33, v119, v123
	v_add3_u32 v30, v30, v124, v128
	v_add3_u32 v31, v31, v125, v129
	v_add3_u32 v32, v32, v126, v130
	v_add3_u32 v33, v33, v127, v131
	v_add3_u32 v30, v30, v132, v136
	v_add3_u32 v31, v31, v133, v137
	v_add3_u32 v32, v32, v134, v138
	v_add3_u32 v33, v33, v135, v139
	v_add3_u32 v30, v30, v140, v144
	v_add3_u32 v31, v31, v141, v145
	v_add3_u32 v32, v32, v142, v146
	v_add3_u32 v33, v33, v143, v147
	v_add3_u32 v30, v30, v148, v152
	v_add3_u32 v31, v31, v149, v153
	v_add3_u32 v32, v32, v150, v154
	v_add3_u32 v33, v33, v151, v155
	v_add3_u32 v30, v30, v156, v160
	v_add3_u32 v31, v31, v157, v161
	v_add3_u32 v32, v32, v158, v162
	v_add3_u32 v33, v33, v159, v163
	v_add3_u32 v30, v30, v164, v168
	v_add3_u32 v31, v31, v165, v169
	v_add3_u32 v32, v32, v166, v170
	v_add3_u32 v33, v33, v167, v171
	v_add3_u32 v30, v30, v172, v176
	v_add3_u32 v31, v31, v173, v177
	v_add3_u32 v32, v32, v174, v178
	v_add3_u32 v33, v33, v175, v179
	v_add3_u32 v30, v30, v180, v184
	v_add3_u32 v31, v31, v181, v185
	v_add3_u32 v32, v32, v182, v186
	v_add3_u32 v33, v33, v183, v187
	v_add3_u32 v30, v30, v188, v192
	v_add3_u32 v31, v31, v189, v193
	v_add3_u32 v32, v32, v190, v194
	v_add3_u32 v33, v33, v191, v195
	s_cmp_gt_i32 s15, 0
	s_cbranch_scc0 .Lbscat_nopre_1
	s_cmp_lt_i32 s15, 64
	s_cbranch_scc0 .Lbscat_nopre_1
	s_cmp_gt_i32 s15, 32
	s_cselect_b32 s16, 1, 0
	v_mad_u32_u24 v10, v68, s16, v10
	v_mad_u32_u24 v11, v69, s16, v11
	v_mad_u32_u24 v12, v70, s16, v12
	v_mad_u32_u24 v13, v71, s16, v13
	s_cmp_gt_i32 s15, 33
	s_cselect_b32 s16, 1, 0
	v_mad_u32_u24 v10, v72, s16, v10
	v_mad_u32_u24 v11, v73, s16, v11
	v_mad_u32_u24 v12, v74, s16, v12
	v_mad_u32_u24 v13, v75, s16, v13
	s_cmp_gt_i32 s15, 34
	s_cselect_b32 s16, 1, 0
	v_mad_u32_u24 v10, v76, s16, v10
	v_mad_u32_u24 v11, v77, s16, v11
	v_mad_u32_u24 v12, v78, s16, v12
	v_mad_u32_u24 v13, v79, s16, v13
	s_cmp_gt_i32 s15, 35
	s_cselect_b32 s16, 1, 0
	v_mad_u32_u24 v10, v80, s16, v10
	v_mad_u32_u24 v11, v81, s16, v11
	v_mad_u32_u24 v12, v82, s16, v12
	v_mad_u32_u24 v13, v83, s16, v13
	s_cmp_gt_i32 s15, 36
	s_cselect_b32 s16, 1, 0
	v_mad_u32_u24 v10, v84, s16, v10
	v_mad_u32_u24 v11, v85, s16, v11
	v_mad_u32_u24 v12, v86, s16, v12
	v_mad_u32_u24 v13, v87, s16, v13
	s_cmp_gt_i32 s15, 37
	s_cselect_b32 s16, 1, 0
	v_mad_u32_u24 v10, v88, s16, v10
	v_mad_u32_u24 v11, v89, s16, v11
	v_mad_u32_u24 v12, v90, s16, v12
	v_mad_u32_u24 v13, v91, s16, v13
	s_cmp_gt_i32 s15, 38
	s_cselect_b32 s16, 1, 0
	v_mad_u32_u24 v10, v92, s16, v10
	v_mad_u32_u24 v11, v93, s16, v11
	v_mad_u32_u24 v12, v94, s16, v12
	v_mad_u32_u24 v13, v95, s16, v13
	s_cmp_gt_i32 s15, 39
	s_cselect_b32 s16, 1, 0
	v_mad_u32_u24 v10, v96, s16, v10
	v_mad_u32_u24 v11, v97, s16, v11
	v_mad_u32_u24 v12, v98, s16, v12
	v_mad_u32_u24 v13, v99, s16, v13
	s_cmp_gt_i32 s15, 40
	s_cselect_b32 s16, 1, 0
	v_mad_u32_u24 v10, v100, s16, v10
	v_mad_u32_u24 v11, v101, s16, v11
	v_mad_u32_u24 v12, v102, s16, v12
	v_mad_u32_u24 v13, v103, s16, v13
	s_cmp_gt_i32 s15, 41
	s_cselect_b32 s16, 1, 0
	v_mad_u32_u24 v10, v104, s16, v10
	v_mad_u32_u24 v11, v105, s16, v11
	v_mad_u32_u24 v12, v106, s16, v12
	v_mad_u32_u24 v13, v107, s16, v13
	s_cmp_gt_i32 s15, 42
	s_cselect_b32 s16, 1, 0
	v_mad_u32_u24 v10, v108, s16, v10
	v_mad_u32_u24 v11, v109, s16, v11
	v_mad_u32_u24 v12, v110, s16, v12
	v_mad_u32_u24 v13, v111, s16, v13
	s_cmp_gt_i32 s15, 43
	s_cselect_b32 s16, 1, 0
	v_mad_u32_u24 v10, v112, s16, v10
	v_mad_u32_u24 v11, v113, s16, v11
	v_mad_u32_u24 v12, v114, s16, v12
	v_mad_u32_u24 v13, v115, s16, v13
	s_cmp_gt_i32 s15, 44
	s_cselect_b32 s16, 1, 0
	v_mad_u32_u24 v10, v116, s16, v10
	v_mad_u32_u24 v11, v117, s16, v11
	v_mad_u32_u24 v12, v118, s16, v12
	v_mad_u32_u24 v13, v119, s16, v13
	s_cmp_gt_i32 s15, 45
	s_cselect_b32 s16, 1, 0
	v_mad_u32_u24 v10, v120, s16, v10
	v_mad_u32_u24 v11, v121, s16, v11
	v_mad_u32_u24 v12, v122, s16, v12
	v_mad_u32_u24 v13, v123, s16, v13
	s_cmp_gt_i32 s15, 46
	s_cselect_b32 s16, 1, 0
	v_mad_u32_u24 v10, v124, s16, v10
	v_mad_u32_u24 v11, v125, s16, v11
	v_mad_u32_u24 v12, v126, s16, v12
	v_mad_u32_u24 v13, v127, s16, v13
	s_cmp_gt_i32 s15, 47
	s_cselect_b32 s16, 1, 0
	v_mad_u32_u24 v10, v128, s16, v10
	v_mad_u32_u24 v11, v129, s16, v11
	v_mad_u32_u24 v12, v130, s16, v12
	v_mad_u32_u24 v13, v131, s16, v13
	s_cmp_gt_i32 s15, 48
	s_cselect_b32 s16, 1, 0
	v_mad_u32_u24 v10, v132, s16, v10
	v_mad_u32_u24 v11, v133, s16, v11
	v_mad_u32_u24 v12, v134, s16, v12
	v_mad_u32_u24 v13, v135, s16, v13
	s_cmp_gt_i32 s15, 49
	s_cselect_b32 s16, 1, 0
	v_mad_u32_u24 v10, v136, s16, v10
	v_mad_u32_u24 v11, v137, s16, v11
	v_mad_u32_u24 v12, v138, s16, v12
	v_mad_u32_u24 v13, v139, s16, v13
	s_cmp_gt_i32 s15, 50
	s_cselect_b32 s16, 1, 0
	v_mad_u32_u24 v10, v140, s16, v10
	v_mad_u32_u24 v11, v141, s16, v11
	v_mad_u32_u24 v12, v142, s16, v12
	v_mad_u32_u24 v13, v143, s16, v13
	s_cmp_gt_i32 s15, 51
	s_cselect_b32 s16, 1, 0
	v_mad_u32_u24 v10, v144, s16, v10
	v_mad_u32_u24 v11, v145, s16, v11
	v_mad_u32_u24 v12, v146, s16, v12
	v_mad_u32_u24 v13, v147, s16, v13
	s_cmp_gt_i32 s15, 52
	s_cselect_b32 s16, 1, 0
	v_mad_u32_u24 v10, v148, s16, v10
	v_mad_u32_u24 v11, v149, s16, v11
	v_mad_u32_u24 v12, v150, s16, v12
	v_mad_u32_u24 v13, v151, s16, v13
	s_cmp_gt_i32 s15, 53
	s_cselect_b32 s16, 1, 0
	v_mad_u32_u24 v10, v152, s16, v10
	v_mad_u32_u24 v11, v153, s16, v11
	v_mad_u32_u24 v12, v154, s16, v12
	v_mad_u32_u24 v13, v155, s16, v13
	s_cmp_gt_i32 s15, 54
	s_cselect_b32 s16, 1, 0
	v_mad_u32_u24 v10, v156, s16, v10
	v_mad_u32_u24 v11, v157, s16, v11
	v_mad_u32_u24 v12, v158, s16, v12
	v_mad_u32_u24 v13, v159, s16, v13
	s_cmp_gt_i32 s15, 55
	s_cselect_b32 s16, 1, 0
	v_mad_u32_u24 v10, v160, s16, v10
	v_mad_u32_u24 v11, v161, s16, v11
	v_mad_u32_u24 v12, v162, s16, v12
	v_mad_u32_u24 v13, v163, s16, v13
	s_cmp_gt_i32 s15, 56
	s_cselect_b32 s16, 1, 0
	v_mad_u32_u24 v10, v164, s16, v10
	v_mad_u32_u24 v11, v165, s16, v11
	v_mad_u32_u24 v12, v166, s16, v12
	v_mad_u32_u24 v13, v167, s16, v13
	s_cmp_gt_i32 s15, 57
	s_cselect_b32 s16, 1, 0
	v_mad_u32_u24 v10, v168, s16, v10
	v_mad_u32_u24 v11, v169, s16, v11
	v_mad_u32_u24 v12, v170, s16, v12
	v_mad_u32_u24 v13, v171, s16, v13
	s_cmp_gt_i32 s15, 58
	s_cselect_b32 s16, 1, 0
	v_mad_u32_u24 v10, v172, s16, v10
	v_mad_u32_u24 v11, v173, s16, v11
	v_mad_u32_u24 v12, v174, s16, v12
	v_mad_u32_u24 v13, v175, s16, v13
	s_cmp_gt_i32 s15, 59
	s_cselect_b32 s16, 1, 0
	v_mad_u32_u24 v10, v176, s16, v10
	v_mad_u32_u24 v11, v177, s16, v11
	v_mad_u32_u24 v12, v178, s16, v12
	v_mad_u32_u24 v13, v179, s16, v13
	s_cmp_gt_i32 s15, 60
	s_cselect_b32 s16, 1, 0
	v_mad_u32_u24 v10, v180, s16, v10
	v_mad_u32_u24 v11, v181, s16, v11
	v_mad_u32_u24 v12, v182, s16, v12
	v_mad_u32_u24 v13, v183, s16, v13
	s_cmp_gt_i32 s15, 61
	s_cselect_b32 s16, 1, 0
	v_mad_u32_u24 v10, v184, s16, v10
	v_mad_u32_u24 v11, v185, s16, v11
	v_mad_u32_u24 v12, v186, s16, v12
	v_mad_u32_u24 v13, v187, s16, v13
	s_cmp_gt_i32 s15, 62
	s_cselect_b32 s16, 1, 0
	v_mad_u32_u24 v10, v188, s16, v10
	v_mad_u32_u24 v11, v189, s16, v11
	v_mad_u32_u24 v12, v190, s16, v12
	v_mad_u32_u24 v13, v191, s16, v13
	s_cmp_gt_i32 s15, 63
	s_cselect_b32 s16, 1, 0
	v_mad_u32_u24 v10, v192, s16, v10
	v_mad_u32_u24 v11, v193, s16, v11
	v_mad_u32_u24 v12, v194, s16, v12
	v_mad_u32_u24 v13, v195, s16, v13
.Lbscat_nopre_1:
	s_cmp_lt_i32 s15, 64
	s_cbranch_scc1 .Lbscat_fin
	v_mov_b32_e32 v10, v30
	v_mov_b32_e32 v11, v31
	v_mov_b32_e32 v12, v32
	v_mov_b32_e32 v13, v33
.Lbscat_fin:
	ds_write_b128 v25, v[30:33] offset:6272
	ds_write_b128 v25, v[10:13]

	.amdhsa_kernel _Z10k_bscatterPKfPKiS2_S2_PiP15HIP_vector_typeIfLj2EEPf
		.amdhsa_group_segment_fixed_size 19228
		.amdhsa_private_segment_fixed_size 0
		.amdhsa_kernarg_size 56
		.amdhsa_user_sgpr_count 2
		.amdhsa_user_sgpr_dispatch_ptr 0
		.amdhsa_user_sgpr_queue_ptr 0
		.amdhsa_user_sgpr_kernarg_segment_ptr 1
		.amdhsa_user_sgpr_dispatch_id 0
		.amdhsa_user_sgpr_kernarg_preload_length 0
		.amdhsa_user_sgpr_kernarg_preload_offset 0
		.amdhsa_user_sgpr_private_segment_size 0
		.amdhsa_uses_dynamic_stack 0
		.amdhsa_enable_private_segment 0
		.amdhsa_system_sgpr_workgroup_id_x 1
		.amdhsa_system_sgpr_workgroup_id_y 0
		.amdhsa_system_sgpr_workgroup_id_z 0
		.amdhsa_system_sgpr_workgroup_info 0
		.amdhsa_system_vgpr_workitem_id 0
		.amdhsa_next_free_vgpr 196
		.amdhsa_next_free_sgpr 20
		.amdhsa_accum_offset 196
		.amdhsa_reserve_vcc 1
		.amdhsa_float_round_mode_32 0
		.amdhsa_float_round_mode_16_64 0
		.amdhsa_float_denorm_mode_32 3
		.amdhsa_float_denorm_mode_16_64 3
		.amdhsa_dx10_clamp 1
		.amdhsa_ieee_mode 1
		.amdhsa_fp16_overflow 0
		.amdhsa_tg_split 0
		.amdhsa_exception_fp_ieee_invalid_op 0
		.amdhsa_exception_fp_denorm_src 0
		.amdhsa_exception_fp_ieee_div_zero 0
		.amdhsa_exception_fp_ieee_overflow 0
		.amdhsa_exception_fp_ieee_underflow 0
		.amdhsa_exception_fp_ieee_inexact 0
		.amdhsa_exception_int_div_zero 0
	.end_amdhsa_kernel

.LBB2_41:
	s_waitcnt lgkmcnt(0)
	s_barrier
	v_readfirstlane_b32 s0, v0
	s_nop 0
	s_cmp_lt_u32 s0, 64
	s_cbranch_scc0 .Lbsort_scan_skip
	v_lshlrev_b32_e32 v12, 3, v0
	ds_read_b64 v[12:13], v12
	s_waitcnt lgkmcnt(0)
	v_add_u32_e32 v14, v12, v13
	v_mov_b32_e32 v11, v14
	v_lshl_add_u32 v10, v0, 2, -4
	ds_bpermute_b32 v10, v10, v14
	v_cmp_le_u32_e32 vcc, 1, v0
	s_waitcnt lgkmcnt(0)
	s_nop 0
	v_cndmask_b32_e32 v10, 0, v10, vcc
	v_add_u32_e32 v14, v14, v10
	v_lshl_add_u32 v10, v0, 2, -8
	ds_bpermute_b32 v10, v10, v14
	v_cmp_le_u32_e32 vcc, 2, v0
	s_waitcnt lgkmcnt(0)
	s_nop 0
	v_cndmask_b32_e32 v10, 0, v10, vcc
	v_add_u32_e32 v14, v14, v10
	v_lshl_add_u32 v10, v0, 2, -16
	ds_bpermute_b32 v10, v10, v14
	v_cmp_le_u32_e32 vcc, 4, v0
	s_waitcnt lgkmcnt(0)
	s_nop 0
	v_cndmask_b32_e32 v10, 0, v10, vcc
	v_add_u32_e32 v14, v14, v10
	s_movk_i32 s0, -32
	v_lshl_add_u32 v10, v0, 2, s0
	ds_bpermute_b32 v10, v10, v14
	v_cmp_le_u32_e32 vcc, 8, v0
	s_waitcnt lgkmcnt(0)
	s_nop 0
	v_cndmask_b32_e32 v10, 0, v10, vcc
	v_add_u32_e32 v14, v14, v10
	s_movk_i32 s0, -64
	v_lshl_add_u32 v10, v0, 2, s0
	ds_bpermute_b32 v10, v10, v14
	v_cmp_le_u32_e32 vcc, 16, v0
	s_waitcnt lgkmcnt(0)
	s_nop 0
	v_cndmask_b32_e32 v10, 0, v10, vcc
	v_add_u32_e32 v14, v14, v10
	s_movk_i32 s0, -128
	v_lshl_add_u32 v10, v0, 2, s0
	ds_bpermute_b32 v10, v10, v14
	v_cmp_le_u32_e32 vcc, 32, v0
	s_waitcnt lgkmcnt(0)
	s_nop 0
	v_cndmask_b32_e32 v10, 0, v10, vcc
	v_add_u32_e32 v14, v14, v10
	v_sub_u32_e32 v10, v14, v11
	v_add_u32_e32 v11, v10, v12
	v_lshlrev_b32_e32 v12, 3, v0
	ds_write_b64 v12, v[10:11] offset:512
.Lbsort_scan_skip:
	v_lshlrev_b32_e32 v10, 2, v0
	v_mov_b32_e32 v11, 0x200
	v_lshl_add_u32 v11, v0, 2, v11
	s_waitcnt lgkmcnt(0)
	s_barrier
	s_and_saveexec_b64 s[0:1], s[4:5]
	s_cbranch_execz .LBB2_74
	ds_read_b32 v12, v10
	ds_read_b32 v13, v11
	v_lshl_or_b32 v10, s2, 7, v0
	s_mov_b32 s4, 0xc351
	v_cmp_gt_i32_e32 vcc, s4, v10
	s_waitcnt lgkmcnt(0)
	v_mov_b32_e32 v12, v13
	ds_write_b32 v11, v12
	s_and_b64 exec, exec, vcc
	s_cbranch_execz .LBB2_74
	v_ashrrev_i32_e32 v11, 31, v10
	v_lshl_add_u64 v[10:11], v[10:11], 2, s[18:19]
	v_add_u32_e32 v12, s14, v12
	global_store_dword v[10:11], v12, off

amdhsa.kernels:
  - .agpr_count:     0
    .args:
      - .actual_access:  read_only
        .address_space:  global
        .offset:         0
        .size:           8
        .value_kind:     global_buffer
      - .actual_access:  write_only
        .address_space:  global
        .offset:         8
        .size:           8
        .value_kind:     global_buffer
      - .offset:         16
        .size:           288
        .value_kind:     by_value
      - .actual_access:  write_only
        .address_space:  global
        .offset:         304
        .size:           8
        .value_kind:     global_buffer
      - .actual_access:  write_only
        .address_space:  global
        .offset:         312
        .size:           8
        .value_kind:     global_buffer
    .group_segment_fixed_size: 1564
    .kernarg_segment_align: 8
    .kernarg_segment_size: 320
    .language:       OpenCL C
    .language_version:
      - 2
      - 0
    .max_flat_workgroup_size: 256
    .name:           _Z8k_bcountPKiPi8PrepArgsPDF16_S3_
    .private_segment_fixed_size: 0
    .sgpr_count:     26
    .sgpr_spill_count: 0
    .symbol:         _Z8k_bcountPKiPi8PrepArgsPDF16_S3_.kd
    .uniform_work_group_size: 1
    .uses_dynamic_stack: false
    .vgpr_count:     26
    .vgpr_spill_count: 0
    .wavefront_size: 64
  - .agpr_count:     0
    .args:
      - .actual_access:  read_only
        .address_space:  global
        .offset:         0
        .size:           8
        .value_kind:     global_buffer
      - .actual_access:  read_only
        .address_space:  global
        .offset:         8
        .size:           8
        .value_kind:     global_buffer
      - .actual_access:  read_only
        .address_space:  global
        .offset:         16
        .size:           8
        .value_kind:     global_buffer
      - .actual_access:  read_only
        .address_space:  global
        .offset:         24
        .size:           8
        .value_kind:     global_buffer
      - .actual_access:  write_only
        .address_space:  global
        .offset:         32
        .size:           8
        .value_kind:     global_buffer
      - .actual_access:  write_only
        .address_space:  global
        .offset:         40
        .size:           8
        .value_kind:     global_buffer
      - .actual_access:  write_only
        .address_space:  global
        .offset:         48
        .size:           8
        .value_kind:     global_buffer
    .group_segment_fixed_size: 19228
    .kernarg_segment_align: 8
    .kernarg_segment_size: 56
    .language:       OpenCL C
    .language_version:
      - 2
      - 0
    .max_flat_workgroup_size: 512
    .name:           _Z10k_bscatterPKfPKiS2_S2_PiP15HIP_vector_typeIfLj2EEPf
    .private_segment_fixed_size: 0
    .sgpr_count:     26
    .sgpr_spill_count: 0
    .symbol:         _Z10k_bscatterPKfPKiS2_S2_PiP15HIP_vector_typeIfLj2EEPf.kd
    .uniform_work_group_size: 1
    .uses_dynamic_stack: false
    .vgpr_count:     196
    .vgpr_spill_count: 0
    .wavefront_size: 64
  - .agpr_count:     0
    .args:
      - .actual_access:  read_only
        .address_space:  global
        .offset:         0
        .size:           8
        .value_kind:     global_buffer
      - .actual_access:  read_only
        .address_space:  global
        .offset:         8
        .size:           8
        .value_kind:     global_buffer
      - .actual_access:  read_only
        .address_space:  global
        .offset:         16
        .size:           8
        .value_kind:     global_buffer
      - .actual_access:  write_only
        .address_space:  global
        .offset:         24
        .size:           8
        .value_kind:     global_buffer
      - .actual_access:  write_only
        .address_space:  global
        .offset:         32
        .size:           8
        .value_kind:     global_buffer
    .group_segment_fixed_size: 1024
    .kernarg_segment_align: 8
    .kernarg_segment_size: 40
    .language:       OpenCL C
    .language_version:
      - 2
      - 0
    .max_flat_workgroup_size: 512
    .name:           _Z7k_bsortPK15HIP_vector_typeIfLj2EEPKiS4_PS_IfLj4EEPi
    .private_segment_fixed_size: 0
    .sgpr_count:     56
    .sgpr_spill_count: 0
    .symbol:         _Z7k_bsortPK15HIP_vector_typeIfLj2EEPKiS4_PS_IfLj4EEPi.kd
    .uniform_work_group_size: 1
    .uses_dynamic_stack: false
    .vgpr_count:     64
    .vgpr_spill_count: 0
    .wavefront_size: 64
  - .agpr_count:     0
    .args:
      - .actual_access:  read_only
        .address_space:  global
        .offset:         0
        .size:           8
        .value_kind:     global_buffer
      - .actual_access:  read_only
        .address_space:  global
        .offset:         8
        .size:           8
        .value_kind:     global_buffer
      - .actual_access:  read_only
        .address_space:  global
        .offset:         16
        .size:           8
        .value_kind:     global_buffer
      - .actual_access:  read_only
        .address_space:  global
        .offset:         24
        .size:           8
        .value_kind:     global_buffer
      - .actual_access:  read_only
        .address_space:  global
        .offset:         32
        .size:           8
        .value_kind:     global_buffer
      - .actual_access:  read_only
        .address_space:  global
        .offset:         40
        .size:           8
        .value_kind:     global_buffer
      - .actual_access:  write_only
        .address_space:  global
        .offset:         48
        .size:           8
        .value_kind:     global_buffer
      - .actual_access:  write_only
        .address_space:  global
        .offset:         56
        .size:           8
        .value_kind:     global_buffer
      - .offset:         64
        .size:           4
        .value_kind:     hidden_block_count_x
      - .offset:         68
        .size:           4
        .value_kind:     hidden_block_count_y
      - .offset:         72
        .size:           4
        .value_kind:     hidden_block_count_z
      - .offset:         76
        .size:           2
        .value_kind:     hidden_group_size_x
      - .offset:         78
        .size:           2
        .value_kind:     hidden_group_size_y
      - .offset:         80
        .size:           2
        .value_kind:     hidden_group_size_z
      - .offset:         82
        .size:           2
        .value_kind:     hidden_remainder_x
      - .offset:         84
        .size:           2
        .value_kind:     hidden_remainder_y
      - .offset:         86
        .size:           2
        .value_kind:     hidden_remainder_z
      - .offset:         104
        .size:           8
        .value_kind:     hidden_global_offset_x
      - .offset:         112
        .size:           8
        .value_kind:     hidden_global_offset_y
      - .offset:         120
        .size:           8
        .value_kind:     hidden_global_offset_z
      - .offset:         128
        .size:           2
        .value_kind:     hidden_grid_dims
    .group_segment_fixed_size: 31488
    .kernarg_segment_align: 8
    .kernarg_segment_size: 320
    .language:       OpenCL C
    .language_version:
      - 2
      - 0
    .max_flat_workgroup_size: 256
    .name:           _Z7k_edge0PK15HIP_vector_typeIfLj4EEPKDv8_DF16_S5_PKfS7_S7_PfS8_
    .private_segment_fixed_size: 0
    .sgpr_count:     59
    .sgpr_spill_count: 0
    .symbol:         _Z7k_edge0PK15HIP_vector_typeIfLj4EEPKDv8_DF16_S5_PKfS7_S7_PfS8_.kd
    .uniform_work_group_size: 1
    .uses_dynamic_stack: false
    .vgpr_count:     96
    .vgpr_spill_count: 0
    .wavefront_size: 64
  - .agpr_count:     0
    .args:
      - .actual_access:  read_only
        .address_space:  global
        .offset:         0
        .size:           8
        .value_kind:     global_buffer
      - .actual_access:  read_only
        .address_space:  global
        .offset:         8
        .size:           8
        .value_kind:     global_buffer
      - .actual_access:  read_only
        .address_space:  global
        .offset:         16
        .size:           8
        .value_kind:     global_buffer
      - .actual_access:  read_only
        .address_space:  global
        .offset:         24
        .size:           8
        .value_kind:     global_buffer
      - .actual_access:  read_only
        .address_space:  global
        .offset:         32
        .size:           8
        .value_kind:     global_buffer
      - .actual_access:  read_only
        .address_space:  global
        .offset:         40
        .size:           8
        .value_kind:     global_buffer
      - .address_space:  global
        .offset:         48
        .size:           8
        .value_kind:     global_buffer
      - .actual_access:  write_only
        .address_space:  global
        .offset:         56
        .size:           8
        .value_kind:     global_buffer
      - .actual_access:  write_only
        .address_space:  global
        .offset:         64
        .size:           8
        .value_kind:     global_buffer
      - .offset:         72
        .size:           4
        .value_kind:     hidden_block_count_x
      - .offset:         76
        .size:           4
        .value_kind:     hidden_block_count_y
      - .offset:         80
        .size:           4
        .value_kind:     hidden_block_count_z
      - .offset:         84
        .size:           2
        .value_kind:     hidden_group_size_x
      - .offset:         86
        .size:           2
        .value_kind:     hidden_group_size_y
      - .offset:         88
        .size:           2
        .value_kind:     hidden_group_size_z
      - .offset:         90
        .size:           2
        .value_kind:     hidden_remainder_x
      - .offset:         92
        .size:           2
        .value_kind:     hidden_remainder_y
      - .offset:         94
        .size:           2
        .value_kind:     hidden_remainder_z
      - .offset:         112
        .size:           8
        .value_kind:     hidden_global_offset_x
      - .offset:         120
        .size:           8
        .value_kind:     hidden_global_offset_y
      - .offset:         128
        .size:           8
        .value_kind:     hidden_global_offset_z
      - .offset:         136
        .size:           2
        .value_kind:     hidden_grid_dims
    .group_segment_fixed_size: 31488
    .kernarg_segment_align: 8
    .kernarg_segment_size: 328
    .language:       OpenCL C
    .language_version:
      - 2
      - 0
    .max_flat_workgroup_size: 256
    .name:           _Z7k_edge1PK15HIP_vector_typeIfLj4EEPKDv8_DF16_S5_PKfS7_S7_PKDv2_DF16_PfSB_
    .private_segment_fixed_size: 0
    .sgpr_count:     56
    .sgpr_spill_count: 0
    .symbol:         _Z7k_edge1PK15HIP_vector_typeIfLj4EEPKDv8_DF16_S5_PKfS7_S7_PKDv2_DF16_PfSB_.kd
    .uniform_work_group_size: 1
    .uses_dynamic_stack: false
    .vgpr_count:     128
    .vgpr_spill_count: 0
    .wavefront_size: 64
  - .agpr_count:     0
    .args:
      - .actual_access:  read_only
        .address_space:  global
        .offset:         0
        .size:           8
        .value_kind:     global_buffer
      - .actual_access:  read_only
        .address_space:  global
        .offset:         8
        .size:           8
        .value_kind:     global_buffer
      - .address_space:  global
        .offset:         16
        .size:           8
        .value_kind:     global_buffer
      - .address_space:  global
        .offset:         24
        .size:           8
        .value_kind:     global_buffer
    .group_segment_fixed_size: 0
    .kernarg_segment_align: 8
    .kernarg_segment_size: 32
    .language:       OpenCL C
    .language_version:
      - 2
      - 0
    .max_flat_workgroup_size: 256
    .name:           _Z6k_poolPKfPKiPfS3_
    .private_segment_fixed_size: 0
    .sgpr_count:     20
    .sgpr_spill_count: 0
    .symbol:         _Z6k_poolPKfPKiPfS3_.kd
    .uniform_work_group_size: 1
    .uses_dynamic_stack: false
    .vgpr_count:     16
    .vgpr_spill_count: 0
    .wavefront_size: 64
  - .agpr_count:     0
    .args:
      - .actual_access:  read_only
        .address_space:  global
        .offset:         0
        .size:           8
        .value_kind:     global_buffer
      - .actual_access:  read_only
        .address_space:  global
        .offset:         8
        .size:           8
        .value_kind:     global_buffer
      - .actual_access:  read_only
        .address_space:  global
        .offset:         16
        .size:           8
        .value_kind:     global_buffer
      - .actual_access:  read_only
        .address_space:  global
        .offset:         24
        .size:           8
        .value_kind:     global_buffer
      - .actual_access:  read_only
        .address_space:  global
        .offset:         32
        .size:           8
        .value_kind:     global_buffer
      - .actual_access:  read_only
        .address_space:  global
        .offset:         40
        .size:           8
        .value_kind:     global_buffer
      - .actual_access:  write_only
        .address_space:  global
        .offset:         48
        .size:           8
        .value_kind:     global_buffer
    .group_segment_fixed_size: 20480
    .kernarg_segment_align: 8
    .kernarg_segment_size: 56
    .language:       OpenCL C
    .language_version:
      - 2
      - 0
    .max_flat_workgroup_size: 64
    .name:           _Z7k_finalPKfS0_S0_S0_S0_S0_Pf
    .private_segment_fixed_size: 0
    .sgpr_count:     42
    .sgpr_spill_count: 0
    .symbol:         _Z7k_finalPKfS0_S0_S0_S0_S0_Pf.kd
    .uniform_work_group_size: 1
    .uses_dynamic_stack: false
    .vgpr_count:     144
    .vgpr_spill_count: 0
    .wavefront_size: 64
  - .agpr_count:     0
    .args:
      - .actual_access:  read_only
        .address_space:  global
        .offset:         0
        .size:           8
        .value_kind:     global_buffer
      - .address_space:  global
        .offset:         8
        .size:           8
        .value_kind:     global_buffer
      - .address_space:  global
        .offset:         16
        .size:           8
        .value_kind:     global_buffer
      - .actual_access:  read_only
        .address_space:  global
        .offset:         24
        .size:           8
        .value_kind:     global_buffer
      - .actual_access:  read_only
        .address_space:  global
        .offset:         32
        .size:           8
        .value_kind:     global_buffer
      - .actual_access:  read_only
        .address_space:  global
        .offset:         40
        .size:           8
        .value_kind:     global_buffer
      - .actual_access:  read_only
        .address_space:  global
        .offset:         48
        .size:           8
        .value_kind:     global_buffer
      - .actual_access:  read_only
        .address_space:  global
        .offset:         56
        .size:           8
        .value_kind:     global_buffer
      - .actual_access:  read_only
        .address_space:  global
        .offset:         64
        .size:           8
        .value_kind:     global_buffer
      - .actual_access:  read_only
        .address_space:  global
        .offset:         72
        .size:           8
        .value_kind:     global_buffer
      - .actual_access:  read_only
        .address_space:  global
        .offset:         80
        .size:           8
        .value_kind:     global_buffer
      - .actual_access:  read_only
        .address_space:  global
        .offset:         88
        .size:           8
        .value_kind:     global_buffer
      - .actual_access:  read_only
        .address_space:  global
        .offset:         96
        .size:           8
        .value_kind:     global_buffer
      - .actual_access:  read_only
        .address_space:  global
        .offset:         104
        .size:           8
        .value_kind:     global_buffer
      - .actual_access:  read_only
        .address_space:  global
        .offset:         112
        .size:           8
        .value_kind:     global_buffer
    .group_segment_fixed_size: 59392
    .kernarg_segment_align: 8
    .kernarg_segment_size: 120
    .language:       OpenCL C
    .language_version:
      - 2
      - 0
    .max_flat_workgroup_size: 256
    .name:           _Z6k_nodeILi0ELi0EEvPfS0_PDv2_DF16_PKiPKfS4_S0_S0_S4_S6_PKDv8_DF16_S6_S9_S6_S9_
    .private_segment_fixed_size: 0
    .sgpr_count:     30
    .sgpr_spill_count: 0
    .symbol:         _Z6k_nodeILi0ELi0EEvPfS0_PDv2_DF16_PKiPKfS4_S0_S0_S4_S6_PKDv8_DF16_S6_S9_S6_S9_.kd
    .uniform_work_group_size: 1
    .uses_dynamic_stack: false
    .vgpr_count:     154
    .vgpr_spill_count: 0
    .wavefront_size: 64
  - .agpr_count:     0
    .args:
      - .actual_access:  read_only
        .address_space:  global
        .offset:         0
        .size:           8
        .value_kind:     global_buffer
      - .address_space:  global
        .offset:         8
        .size:           8
        .value_kind:     global_buffer
      - .address_space:  global
        .offset:         16
        .size:           8
        .value_kind:     global_buffer
      - .actual_access:  read_only
        .address_space:  global
        .offset:         24
        .size:           8
        .value_kind:     global_buffer
      - .actual_access:  read_only
        .address_space:  global
        .offset:         32
        .size:           8
        .value_kind:     global_buffer
      - .actual_access:  read_only
        .address_space:  global
        .offset:         40
        .size:           8
        .value_kind:     global_buffer
      - .actual_access:  read_only
        .address_space:  global
        .offset:         48
        .size:           8
        .value_kind:     global_buffer
      - .actual_access:  read_only
        .address_space:  global
        .offset:         56
        .size:           8
        .value_kind:     global_buffer
      - .actual_access:  read_only
        .address_space:  global
        .offset:         64
        .size:           8
        .value_kind:     global_buffer
      - .actual_access:  read_only
        .address_space:  global
        .offset:         72
        .size:           8
        .value_kind:     global_buffer
      - .actual_access:  read_only
        .address_space:  global
        .offset:         80
        .size:           8
        .value_kind:     global_buffer
      - .actual_access:  read_only
        .address_space:  global
        .offset:         88
        .size:           8
        .value_kind:     global_buffer
      - .actual_access:  read_only
        .address_space:  global
        .offset:         96
        .size:           8
        .value_kind:     global_buffer
      - .actual_access:  read_only
        .address_space:  global
        .offset:         104
        .size:           8
        .value_kind:     global_buffer
      - .actual_access:  read_only
        .address_space:  global
        .offset:         112
        .size:           8
        .value_kind:     global_buffer
    .group_segment_fixed_size: 59392
    .kernarg_segment_align: 8
    .kernarg_segment_size: 120
    .language:       OpenCL C
    .language_version:
      - 2
      - 0
    .max_flat_workgroup_size: 256
    .name:           _Z6k_nodeILi1ELi0EEvPfS0_PDv2_DF16_PKiPKfS4_S0_S0_S4_S6_PKDv8_DF16_S6_S9_S6_S9_
    .private_segment_fixed_size: 0
    .sgpr_count:     30
    .sgpr_spill_count: 0
    .symbol:         _Z6k_nodeILi1ELi0EEvPfS0_PDv2_DF16_PKiPKfS4_S0_S0_S4_S6_PKDv8_DF16_S6_S9_S6_S9_.kd
    .uniform_work_group_size: 1
    .uses_dynamic_stack: false
    .vgpr_count:     220
    .vgpr_spill_count: 0
    .wavefront_size: 64
  - .agpr_count:     0
    .args:
      - .actual_access:  read_only
        .address_space:  global
        .offset:         0
        .size:           8
        .value_kind:     global_buffer
      - .actual_access:  read_only
        .address_space:  global
        .offset:         8
        .size:           8
        .value_kind:     global_buffer
      - .address_space:  global
        .offset:         16
        .size:           8
        .value_kind:     global_buffer
      - .actual_access:  read_only
        .address_space:  global
        .offset:         24
        .size:           8
        .value_kind:     global_buffer
      - .actual_access:  read_only
        .address_space:  global
        .offset:         32
        .size:           8
        .value_kind:     global_buffer
      - .actual_access:  read_only
        .address_space:  global
        .offset:         40
        .size:           8
        .value_kind:     global_buffer
      - .address_space:  global
        .offset:         48
        .size:           8
        .value_kind:     global_buffer
      - .address_space:  global
        .offset:         56
        .size:           8
        .value_kind:     global_buffer
      - .actual_access:  read_only
        .address_space:  global
        .offset:         64
        .size:           8
        .value_kind:     global_buffer
      - .actual_access:  read_only
        .address_space:  global
        .offset:         72
        .size:           8
        .value_kind:     global_buffer
      - .actual_access:  read_only
        .address_space:  global
        .offset:         80
        .size:           8
        .value_kind:     global_buffer
      - .actual_access:  read_only
        .address_space:  global
        .offset:         88
        .size:           8
        .value_kind:     global_buffer
      - .actual_access:  read_only
        .address_space:  global
        .offset:         96
        .size:           8
        .value_kind:     global_buffer
      - .actual_access:  read_only
        .address_space:  global
        .offset:         104
        .size:           8
        .value_kind:     global_buffer
      - .actual_access:  read_only
        .address_space:  global
        .offset:         112
        .size:           8
        .value_kind:     global_buffer
    .group_segment_fixed_size: 59392
    .kernarg_segment_align: 8
    .kernarg_segment_size: 120
    .language:       OpenCL C
    .language_version:
      - 2
      - 0
    .max_flat_workgroup_size: 256
    .name:           _Z6k_nodeILi1ELi1EEvPfS0_PDv2_DF16_PKiPKfS4_S0_S0_S4_S6_PKDv8_DF16_S6_S9_S6_S9_
    .private_segment_fixed_size: 0
    .sgpr_count:     30
    .sgpr_spill_count: 0
    .symbol:         _Z6k_nodeILi1ELi1EEvPfS0_PDv2_DF16_PKiPKfS4_S0_S0_S4_S6_PKDv8_DF16_S6_S9_S6_S9_.kd
    .uniform_work_group_size: 1
    .uses_dynamic_stack: false
    .vgpr_count:     220
    .vgpr_spill_count: 0
    .wavefront_size: 64
